# v57 plus gate-byte stores of the gate GEMM epilogue written with the default cache policy (they are re-read by the next phase)
# baseline (speedup 1.0000x reference)
.LBB0_781:
	v_lshl_or_b32 v0, s10, 8, v172
	v_ashrrev_i32_e32 v1, 31, v0
	v_lshl_add_u64 v[20:21], v[0:1], 2, s[36:37]
	s_nop 15
	global_load_dwordx4 v[0:3], v[20:21], off offset:16
	global_load_dwordx4 v[4:7], v[20:21], off
	s_mov_b32 s2, 0xbfb8aa3b
	s_waitcnt vmcnt(0)
	v_pk_mul_f32 v[8:9], v[2:3], s[2:3] op_sel_hi:[1,0]
	v_pk_mul_f32 v[12:13], v[0:1], s[2:3] op_sel_hi:[1,0]
	global_load_dwordx4 v[16:19], v[20:21], off offset:528
	global_load_dwordx4 v[0:3], v[20:21], off offset:512
	v_pk_mul_f32 v[14:15], v[4:5], s[2:3] op_sel_hi:[1,0]
	v_pk_mul_f32 v[10:11], v[6:7], s[2:3] op_sel_hi:[1,0]
	v_fmamk_f32 v20, v157, 0xbb38aa3b, v15
	v_exp_f32_e32 v20, v20
	s_waitcnt vmcnt(0)
	v_pk_mul_f32 v[4:5], v[16:17], s[2:3] op_sel_hi:[1,0]
	v_pk_mul_f32 v[6:7], v[0:1], s[2:3] op_sel_hi:[1,0]
	v_pk_mul_f32 v[0:1], v[18:19], s[2:3] op_sel_hi:[1,0]
	v_fmamk_f32 v18, v156, 0xbb38aa3b, v14
	v_exp_f32_e32 v18, v18
	v_min_f32_e32 v20, 0x437e0000, v20
	v_fmamk_f32 v20, v20, 0x3b808081, v245
	v_rcp_f32_e32 v20, v20
	v_min_f32_e32 v18, 0x437e0000, v18
	v_fmamk_f32 v18, v18, 0x3b808081, v245
	v_rcp_f32_e32 v18, v18
	v_fmamk_f32 v19, v152, 0xbb38aa3b, v12
	v_exp_f32_e32 v19, v19
	v_pk_mul_f32 v[2:3], v[2:3], s[2:3] op_sel_hi:[1,0]
	v_cvt_pk_u8_f32 v18, v18, 0, 0
	v_cvt_pk_u8_f32 v18, v20, 1, v18
	v_fmamk_f32 v20, v153, 0xbb38aa3b, v13
	v_exp_f32_e32 v20, v20
	v_min_f32_e32 v19, 0x437e0000, v19
	v_fmamk_f32 v19, v19, 0x3b808081, v245
	v_rcp_f32_e32 v19, v19
	v_min_f32_e32 v20, 0x437e0000, v20
	v_fmamk_f32 v20, v20, 0x3b808081, v245
	v_rcp_f32_e32 v20, v20
	v_cvt_pk_u8_f32 v19, v19, 0, 0
	s_lshl_b32 s2, s11, 4
	s_add_i32 s2, s2, s10
	v_cvt_pk_u8_f32 v19, v20, 1, v19
	v_fmamk_f32 v20, v158, 0xbb38aa3b, v10
	v_exp_f32_e32 v20, v20
	s_ashr_i32 s3, s2, 31
	s_lshl_b64 s[2:3], s[2:3], 16
	v_lshl_add_u64 v[16:17], v[164:165], 0, s[2:3]
	v_min_f32_e32 v20, 0x437e0000, v20
	v_fmamk_f32 v20, v20, 0x3b808081, v245
	v_rcp_f32_e32 v20, v20
	s_movk_i32 s2, 0x1000
	v_cvt_pk_u8_f32 v18, v20, 2, v18
	v_fmamk_f32 v20, v154, 0xbb38aa3b, v8
	v_exp_f32_e32 v20, v20
	s_nop 0
	v_min_f32_e32 v20, 0x437e0000, v20
	v_fmamk_f32 v20, v20, 0x3b808081, v245
	v_rcp_f32_e32 v20, v20
	s_nop 0
	v_cvt_pk_u8_f32 v19, v20, 2, v19
	v_fmamk_f32 v20, v159, 0xbb38aa3b, v11
	v_exp_f32_e32 v20, v20
	s_nop 0
	v_min_f32_e32 v20, 0x437e0000, v20
	v_fmamk_f32 v20, v20, 0x3b808081, v245
	v_rcp_f32_e32 v20, v20
	s_nop 0
	v_cvt_pk_u8_f32 v18, v20, 3, v18
	v_fmamk_f32 v20, v155, 0xbb38aa3b, v9
	v_exp_f32_e32 v20, v20
	s_nop 0
	v_min_f32_e32 v20, 0x437e0000, v20
	v_fmamk_f32 v20, v20, 0x3b808081, v245
	v_rcp_f32_e32 v20, v20
	s_nop 0
	v_cvt_pk_u8_f32 v19, v20, 3, v19
	global_store_dwordx2 v[16:17], v[18:19], off
	v_fmamk_f32 v18, v148, 0xbb38aa3b, v6
	v_exp_f32_e32 v18, v18
	v_fmamk_f32 v20, v149, 0xbb38aa3b, v7
	v_exp_f32_e32 v20, v20
	v_fmamk_f32 v19, v144, 0xbb38aa3b, v4
	v_min_f32_e32 v18, 0x437e0000, v18
	v_fmamk_f32 v18, v18, 0x3b808081, v245
	v_min_f32_e32 v20, 0x437e0000, v20
	v_rcp_f32_e32 v18, v18
	v_fmamk_f32 v20, v20, 0x3b808081, v245
	v_rcp_f32_e32 v20, v20
	v_exp_f32_e32 v19, v19
	v_cvt_pk_u8_f32 v18, v18, 0, 0
	v_cvt_pk_u8_f32 v18, v20, 1, v18
	v_fmamk_f32 v20, v145, 0xbb38aa3b, v5
	v_exp_f32_e32 v20, v20
	v_min_f32_e32 v19, 0x437e0000, v19
	v_fmamk_f32 v19, v19, 0x3b808081, v245
	v_rcp_f32_e32 v19, v19
	v_min_f32_e32 v20, 0x437e0000, v20
	v_fmamk_f32 v20, v20, 0x3b808081, v245
	v_rcp_f32_e32 v20, v20
	v_cvt_pk_u8_f32 v19, v19, 0, 0
	v_cvt_pk_u8_f32 v19, v20, 1, v19
	v_fmamk_f32 v20, v150, 0xbb38aa3b, v2
	v_exp_f32_e32 v20, v20
	s_nop 0
	v_min_f32_e32 v20, 0x437e0000, v20
	v_fmamk_f32 v20, v20, 0x3b808081, v245
	v_rcp_f32_e32 v20, v20
	s_nop 0
	v_cvt_pk_u8_f32 v18, v20, 2, v18
	v_fmamk_f32 v20, v146, 0xbb38aa3b, v0
	v_exp_f32_e32 v20, v20
	s_nop 0
	v_min_f32_e32 v20, 0x437e0000, v20
	v_fmamk_f32 v20, v20, 0x3b808081, v245
	v_rcp_f32_e32 v20, v20
	s_nop 0
	v_cvt_pk_u8_f32 v19, v20, 2, v19
	v_fmamk_f32 v20, v151, 0xbb38aa3b, v3
	v_exp_f32_e32 v20, v20
	s_nop 0
	v_min_f32_e32 v20, 0x437e0000, v20
	v_fmamk_f32 v20, v20, 0x3b808081, v245
	v_rcp_f32_e32 v20, v20
	s_nop 0
	v_cvt_pk_u8_f32 v18, v20, 3, v18
	v_fmamk_f32 v20, v147, 0xbb38aa3b, v1
	v_exp_f32_e32 v20, v20
	s_nop 0
	v_min_f32_e32 v20, 0x437e0000, v20
	v_fmamk_f32 v20, v20, 0x3b808081, v245
	v_rcp_f32_e32 v20, v20
	s_nop 0
	v_cvt_pk_u8_f32 v19, v20, 3, v19
	global_store_dwordx2 v[16:17], v[18:19], off offset:512
	v_fmamk_f32 v18, v140, 0xbb38aa3b, v14
	v_exp_f32_e32 v18, v18
	v_fmamk_f32 v20, v141, 0xbb38aa3b, v15
	v_exp_f32_e32 v20, v20
	v_fmamk_f32 v19, v136, 0xbb38aa3b, v12
	v_min_f32_e32 v18, 0x437e0000, v18
	v_fmamk_f32 v18, v18, 0x3b808081, v245
	v_min_f32_e32 v20, 0x437e0000, v20
	v_rcp_f32_e32 v18, v18
	v_fmamk_f32 v20, v20, 0x3b808081, v245
	v_rcp_f32_e32 v20, v20
	v_exp_f32_e32 v19, v19
	v_cvt_pk_u8_f32 v18, v18, 0, 0
	v_cvt_pk_u8_f32 v18, v20, 1, v18
	v_fmamk_f32 v20, v137, 0xbb38aa3b, v13
	v_exp_f32_e32 v20, v20
	v_min_f32_e32 v19, 0x437e0000, v19
	v_fmamk_f32 v19, v19, 0x3b808081, v245
	v_rcp_f32_e32 v19, v19
	v_min_f32_e32 v20, 0x437e0000, v20
	v_fmamk_f32 v20, v20, 0x3b808081, v245
	v_rcp_f32_e32 v20, v20
	v_cvt_pk_u8_f32 v19, v19, 0, 0
	v_cvt_pk_u8_f32 v19, v20, 1, v19
	v_fmamk_f32 v20, v142, 0xbb38aa3b, v10
	v_exp_f32_e32 v20, v20
	s_nop 0
	v_min_f32_e32 v20, 0x437e0000, v20
	v_fmamk_f32 v20, v20, 0x3b808081, v245
	v_rcp_f32_e32 v20, v20
	s_nop 0
	v_cvt_pk_u8_f32 v18, v20, 2, v18
	v_fmamk_f32 v20, v138, 0xbb38aa3b, v8
	v_exp_f32_e32 v20, v20
	s_nop 0
	v_min_f32_e32 v20, 0x437e0000, v20
	v_fmamk_f32 v20, v20, 0x3b808081, v245
	v_rcp_f32_e32 v20, v20
	s_nop 0
	v_cvt_pk_u8_f32 v19, v20, 2, v19
	v_fmamk_f32 v20, v143, 0xbb38aa3b, v11
	v_exp_f32_e32 v20, v20
	s_nop 0
	v_min_f32_e32 v20, 0x437e0000, v20
	v_fmamk_f32 v20, v20, 0x3b808081, v245
	v_rcp_f32_e32 v20, v20
	s_nop 0
	v_cvt_pk_u8_f32 v18, v20, 3, v18
	v_fmamk_f32 v20, v139, 0xbb38aa3b, v9
	v_exp_f32_e32 v20, v20
	s_nop 0
	v_min_f32_e32 v20, 0x437e0000, v20
	v_fmamk_f32 v20, v20, 0x3b808081, v245
	v_rcp_f32_e32 v20, v20
	s_nop 0
	v_cvt_pk_u8_f32 v19, v20, 3, v19
	global_store_dwordx2 v[16:17], v[18:19], off offset:1024
	v_fmamk_f32 v18, v132, 0xbb38aa3b, v6
	v_exp_f32_e32 v18, v18
	v_fmamk_f32 v20, v133, 0xbb38aa3b, v7
	v_exp_f32_e32 v20, v20
	v_fmamk_f32 v19, v128, 0xbb38aa3b, v4
	v_min_f32_e32 v18, 0x437e0000, v18
	v_fmamk_f32 v18, v18, 0x3b808081, v245
	v_min_f32_e32 v20, 0x437e0000, v20
	v_rcp_f32_e32 v18, v18
	v_fmamk_f32 v20, v20, 0x3b808081, v245
	v_rcp_f32_e32 v20, v20
	v_exp_f32_e32 v19, v19
	v_cvt_pk_u8_f32 v18, v18, 0, 0
	v_cvt_pk_u8_f32 v18, v20, 1, v18
	v_fmamk_f32 v20, v129, 0xbb38aa3b, v5
	v_exp_f32_e32 v20, v20
	v_min_f32_e32 v19, 0x437e0000, v19
	v_fmamk_f32 v19, v19, 0x3b808081, v245
	v_rcp_f32_e32 v19, v19
	v_min_f32_e32 v20, 0x437e0000, v20
	v_fmamk_f32 v20, v20, 0x3b808081, v245
	v_rcp_f32_e32 v20, v20
	v_cvt_pk_u8_f32 v19, v19, 0, 0
	v_cvt_pk_u8_f32 v19, v20, 1, v19
	v_fmamk_f32 v20, v134, 0xbb38aa3b, v2
	v_exp_f32_e32 v20, v20
	s_nop 0
	v_min_f32_e32 v20, 0x437e0000, v20
	v_fmamk_f32 v20, v20, 0x3b808081, v245
	v_rcp_f32_e32 v20, v20
	s_nop 0
	v_cvt_pk_u8_f32 v18, v20, 2, v18
	v_fmamk_f32 v20, v130, 0xbb38aa3b, v0
	v_exp_f32_e32 v20, v20
	s_nop 0
	v_min_f32_e32 v20, 0x437e0000, v20
	v_fmamk_f32 v20, v20, 0x3b808081, v245
	v_rcp_f32_e32 v20, v20
	s_nop 0
	v_cvt_pk_u8_f32 v19, v20, 2, v19
	v_fmamk_f32 v20, v135, 0xbb38aa3b, v3
	v_exp_f32_e32 v20, v20
	s_nop 0
	v_min_f32_e32 v20, 0x437e0000, v20
	v_fmamk_f32 v20, v20, 0x3b808081, v245
	v_rcp_f32_e32 v20, v20
	s_nop 0
	v_cvt_pk_u8_f32 v18, v20, 3, v18
	v_fmamk_f32 v20, v131, 0xbb38aa3b, v1
	v_exp_f32_e32 v20, v20
	s_nop 0
	v_min_f32_e32 v20, 0x437e0000, v20
	v_fmamk_f32 v20, v20, 0x3b808081, v245
	v_rcp_f32_e32 v20, v20
	s_nop 0
	v_cvt_pk_u8_f32 v19, v20, 3, v19
	global_store_dwordx2 v[16:17], v[18:19], off offset:1536
	v_fmamk_f32 v18, v124, 0xbb38aa3b, v14
	v_exp_f32_e32 v18, v18
	v_fmamk_f32 v20, v125, 0xbb38aa3b, v15
	v_exp_f32_e32 v20, v20
	v_fmamk_f32 v19, v120, 0xbb38aa3b, v12
	v_min_f32_e32 v18, 0x437e0000, v18
	v_fmamk_f32 v18, v18, 0x3b808081, v245
	v_min_f32_e32 v20, 0x437e0000, v20
	v_rcp_f32_e32 v18, v18
	v_fmamk_f32 v20, v20, 0x3b808081, v245
	v_rcp_f32_e32 v20, v20
	v_exp_f32_e32 v19, v19
	v_cvt_pk_u8_f32 v18, v18, 0, 0
	v_cvt_pk_u8_f32 v18, v20, 1, v18
	v_fmamk_f32 v20, v121, 0xbb38aa3b, v13
	v_exp_f32_e32 v20, v20
	v_min_f32_e32 v19, 0x437e0000, v19
	v_fmamk_f32 v19, v19, 0x3b808081, v245
	v_rcp_f32_e32 v19, v19
	v_min_f32_e32 v20, 0x437e0000, v20
	v_fmamk_f32 v20, v20, 0x3b808081, v245
	v_rcp_f32_e32 v20, v20
	v_cvt_pk_u8_f32 v19, v19, 0, 0
	v_cvt_pk_u8_f32 v19, v20, 1, v19
	v_fmamk_f32 v20, v126, 0xbb38aa3b, v10
	v_exp_f32_e32 v20, v20
	s_nop 0
	v_min_f32_e32 v20, 0x437e0000, v20
	v_fmamk_f32 v20, v20, 0x3b808081, v245
	v_rcp_f32_e32 v20, v20
	s_nop 0
	v_cvt_pk_u8_f32 v18, v20, 2, v18
	v_fmamk_f32 v20, v122, 0xbb38aa3b, v8
	v_exp_f32_e32 v20, v20
	s_nop 0
	v_min_f32_e32 v20, 0x437e0000, v20
	v_fmamk_f32 v20, v20, 0x3b808081, v245
	v_rcp_f32_e32 v20, v20
	s_nop 0
	v_cvt_pk_u8_f32 v19, v20, 2, v19
	v_fmamk_f32 v20, v127, 0xbb38aa3b, v11
	v_exp_f32_e32 v20, v20
	s_nop 0
	v_min_f32_e32 v20, 0x437e0000, v20
	v_fmamk_f32 v20, v20, 0x3b808081, v245
	v_rcp_f32_e32 v20, v20
	s_nop 0
	v_cvt_pk_u8_f32 v18, v20, 3, v18
	v_fmamk_f32 v20, v123, 0xbb38aa3b, v9
	v_exp_f32_e32 v20, v20
	s_nop 0
	v_min_f32_e32 v20, 0x437e0000, v20
	v_fmamk_f32 v20, v20, 0x3b808081, v245
	v_rcp_f32_e32 v20, v20
	s_nop 0
	v_cvt_pk_u8_f32 v19, v20, 3, v19
	global_store_dwordx2 v[16:17], v[18:19], off offset:2048
	v_fmamk_f32 v18, v116, 0xbb38aa3b, v6
	v_exp_f32_e32 v18, v18
	v_fmamk_f32 v20, v117, 0xbb38aa3b, v7
	v_exp_f32_e32 v20, v20
	v_fmamk_f32 v19, v112, 0xbb38aa3b, v4
	v_min_f32_e32 v18, 0x437e0000, v18
	v_fmamk_f32 v18, v18, 0x3b808081, v245
	v_min_f32_e32 v20, 0x437e0000, v20
	v_rcp_f32_e32 v18, v18
	v_fmamk_f32 v20, v20, 0x3b808081, v245
	v_rcp_f32_e32 v20, v20
	v_exp_f32_e32 v19, v19
	v_cvt_pk_u8_f32 v18, v18, 0, 0
	v_cvt_pk_u8_f32 v18, v20, 1, v18
	v_fmamk_f32 v20, v113, 0xbb38aa3b, v5
	v_exp_f32_e32 v20, v20
	v_min_f32_e32 v19, 0x437e0000, v19
	v_fmamk_f32 v19, v19, 0x3b808081, v245
	v_rcp_f32_e32 v19, v19
	v_min_f32_e32 v20, 0x437e0000, v20
	v_fmamk_f32 v20, v20, 0x3b808081, v245
	v_rcp_f32_e32 v20, v20
	v_cvt_pk_u8_f32 v19, v19, 0, 0
	v_cvt_pk_u8_f32 v19, v20, 1, v19
	v_fmamk_f32 v20, v118, 0xbb38aa3b, v2
	v_exp_f32_e32 v20, v20
	s_nop 0
	v_min_f32_e32 v20, 0x437e0000, v20
	v_fmamk_f32 v20, v20, 0x3b808081, v245
	v_rcp_f32_e32 v20, v20
	s_nop 0
	v_cvt_pk_u8_f32 v18, v20, 2, v18
	v_fmamk_f32 v20, v114, 0xbb38aa3b, v0
	v_exp_f32_e32 v20, v20
	s_nop 0
	v_min_f32_e32 v20, 0x437e0000, v20
	v_fmamk_f32 v20, v20, 0x3b808081, v245
	v_rcp_f32_e32 v20, v20
	s_nop 0
	v_cvt_pk_u8_f32 v19, v20, 2, v19
	v_fmamk_f32 v20, v119, 0xbb38aa3b, v3
	v_exp_f32_e32 v20, v20
	s_nop 0
	v_min_f32_e32 v20, 0x437e0000, v20
	v_fmamk_f32 v20, v20, 0x3b808081, v245
	v_rcp_f32_e32 v20, v20
	s_nop 0
	v_cvt_pk_u8_f32 v18, v20, 3, v18
	v_fmamk_f32 v20, v115, 0xbb38aa3b, v1
	v_exp_f32_e32 v20, v20
	s_nop 0
	v_min_f32_e32 v20, 0x437e0000, v20
	v_fmamk_f32 v20, v20, 0x3b808081, v245
	v_rcp_f32_e32 v20, v20
	s_nop 0
	v_cvt_pk_u8_f32 v19, v20, 3, v19
	global_store_dwordx2 v[16:17], v[18:19], off offset:2560
	v_fmamk_f32 v18, v108, 0xbb38aa3b, v14
	v_exp_f32_e32 v18, v18
	v_fmamk_f32 v20, v109, 0xbb38aa3b, v15
	v_exp_f32_e32 v20, v20
	v_fmamk_f32 v19, v104, 0xbb38aa3b, v12
	v_min_f32_e32 v18, 0x437e0000, v18
	v_fmamk_f32 v18, v18, 0x3b808081, v245
	v_min_f32_e32 v20, 0x437e0000, v20
	v_rcp_f32_e32 v18, v18
	v_fmamk_f32 v20, v20, 0x3b808081, v245
	v_rcp_f32_e32 v20, v20
	v_exp_f32_e32 v19, v19
	v_cvt_pk_u8_f32 v18, v18, 0, 0
	v_cvt_pk_u8_f32 v18, v20, 1, v18
	v_fmamk_f32 v20, v105, 0xbb38aa3b, v13
	v_exp_f32_e32 v20, v20
	v_min_f32_e32 v19, 0x437e0000, v19
	v_fmamk_f32 v19, v19, 0x3b808081, v245
	v_rcp_f32_e32 v19, v19
	v_min_f32_e32 v20, 0x437e0000, v20
	v_fmamk_f32 v20, v20, 0x3b808081, v245
	v_rcp_f32_e32 v20, v20
	v_cvt_pk_u8_f32 v19, v19, 0, 0
	v_cvt_pk_u8_f32 v19, v20, 1, v19
	v_fmamk_f32 v20, v110, 0xbb38aa3b, v10
	v_exp_f32_e32 v20, v20
	s_nop 0
	v_min_f32_e32 v20, 0x437e0000, v20
	v_fmamk_f32 v20, v20, 0x3b808081, v245
	v_rcp_f32_e32 v20, v20
	s_nop 0
	v_cvt_pk_u8_f32 v18, v20, 2, v18
	v_fmamk_f32 v20, v106, 0xbb38aa3b, v8
	v_exp_f32_e32 v20, v20
	s_nop 0
	v_min_f32_e32 v20, 0x437e0000, v20
	v_fmamk_f32 v20, v20, 0x3b808081, v245
	v_rcp_f32_e32 v20, v20
	s_nop 0
	v_cvt_pk_u8_f32 v19, v20, 2, v19
	v_fmamk_f32 v20, v111, 0xbb38aa3b, v11
	v_exp_f32_e32 v20, v20
	s_nop 0
	v_min_f32_e32 v20, 0x437e0000, v20
	v_fmamk_f32 v20, v20, 0x3b808081, v245
	v_rcp_f32_e32 v20, v20
	s_nop 0
	v_cvt_pk_u8_f32 v18, v20, 3, v18
	v_fmamk_f32 v20, v107, 0xbb38aa3b, v9
	v_exp_f32_e32 v20, v20
	s_nop 0
	v_min_f32_e32 v20, 0x437e0000, v20
	v_fmamk_f32 v20, v20, 0x3b808081, v245
	v_rcp_f32_e32 v20, v20
	s_nop 0
	v_cvt_pk_u8_f32 v19, v20, 3, v19
	global_store_dwordx2 v[16:17], v[18:19], off offset:3072
	v_fmamk_f32 v18, v100, 0xbb38aa3b, v6
	v_exp_f32_e32 v18, v18
	v_fmamk_f32 v20, v101, 0xbb38aa3b, v7
	v_exp_f32_e32 v20, v20
	v_fmamk_f32 v19, v96, 0xbb38aa3b, v4
	v_min_f32_e32 v18, 0x437e0000, v18
	v_fmamk_f32 v18, v18, 0x3b808081, v245
	v_min_f32_e32 v20, 0x437e0000, v20
	v_rcp_f32_e32 v18, v18
	v_fmamk_f32 v20, v20, 0x3b808081, v245
	v_rcp_f32_e32 v20, v20
	v_exp_f32_e32 v19, v19
	v_cvt_pk_u8_f32 v18, v18, 0, 0
	v_cvt_pk_u8_f32 v18, v20, 1, v18
	v_fmamk_f32 v20, v97, 0xbb38aa3b, v5
	v_exp_f32_e32 v20, v20
	v_min_f32_e32 v19, 0x437e0000, v19
	v_fmamk_f32 v19, v19, 0x3b808081, v245
	v_rcp_f32_e32 v19, v19
	v_min_f32_e32 v20, 0x437e0000, v20
	v_fmamk_f32 v20, v20, 0x3b808081, v245
	v_rcp_f32_e32 v20, v20
	v_cvt_pk_u8_f32 v19, v19, 0, 0
	v_cvt_pk_u8_f32 v19, v20, 1, v19
	v_fmamk_f32 v20, v102, 0xbb38aa3b, v2
	v_exp_f32_e32 v20, v20
	s_nop 0
	v_min_f32_e32 v20, 0x437e0000, v20
	v_fmamk_f32 v20, v20, 0x3b808081, v245
	v_rcp_f32_e32 v20, v20
	s_nop 0
	v_cvt_pk_u8_f32 v18, v20, 2, v18
	v_fmamk_f32 v20, v98, 0xbb38aa3b, v0
	v_exp_f32_e32 v20, v20
	s_nop 0
	v_min_f32_e32 v20, 0x437e0000, v20
	v_fmamk_f32 v20, v20, 0x3b808081, v245
	v_rcp_f32_e32 v20, v20
	s_nop 0
	v_cvt_pk_u8_f32 v19, v20, 2, v19
	v_fmamk_f32 v20, v103, 0xbb38aa3b, v3
	v_exp_f32_e32 v20, v20
	s_nop 0
	v_min_f32_e32 v20, 0x437e0000, v20
	v_fmamk_f32 v20, v20, 0x3b808081, v245
	v_rcp_f32_e32 v20, v20
	s_nop 0
	v_cvt_pk_u8_f32 v18, v20, 3, v18
	v_fmamk_f32 v20, v99, 0xbb38aa3b, v1
	v_exp_f32_e32 v20, v20
	s_nop 0
	v_min_f32_e32 v20, 0x437e0000, v20
	v_fmamk_f32 v20, v20, 0x3b808081, v245
	v_rcp_f32_e32 v20, v20
	s_nop 0
	v_cvt_pk_u8_f32 v19, v20, 3, v19
	global_store_dwordx2 v[16:17], v[18:19], off offset:3584
	v_fmamk_f32 v18, v92, 0xbb38aa3b, v14
	v_exp_f32_e32 v18, v18
	v_fmamk_f32 v20, v93, 0xbb38aa3b, v15
	v_exp_f32_e32 v20, v20
	v_fmamk_f32 v19, v88, 0xbb38aa3b, v12
	v_min_f32_e32 v18, 0x437e0000, v18
	v_fmamk_f32 v18, v18, 0x3b808081, v245
	v_min_f32_e32 v20, 0x437e0000, v20
	v_rcp_f32_e32 v18, v18
	v_fmamk_f32 v20, v20, 0x3b808081, v245
	v_rcp_f32_e32 v20, v20
	v_exp_f32_e32 v19, v19
	v_cvt_pk_u8_f32 v18, v18, 0, 0
	v_add_co_u32_e32 v16, vcc, s2, v16
	v_cvt_pk_u8_f32 v18, v20, 1, v18
	v_fmamk_f32 v20, v89, 0xbb38aa3b, v13
	v_exp_f32_e32 v20, v20
	v_min_f32_e32 v19, 0x437e0000, v19
	v_fmamk_f32 v19, v19, 0x3b808081, v245
	v_rcp_f32_e32 v19, v19
	v_min_f32_e32 v20, 0x437e0000, v20
	v_fmamk_f32 v20, v20, 0x3b808081, v245
	v_rcp_f32_e32 v20, v20
	v_cvt_pk_u8_f32 v19, v19, 0, 0
	v_addc_co_u32_e32 v17, vcc, 0, v17, vcc
	v_cvt_pk_u8_f32 v19, v20, 1, v19
	v_fmamk_f32 v20, v94, 0xbb38aa3b, v10
	v_exp_f32_e32 v20, v20
	s_mov_b64 s[2:3], -1
	s_andn2_b64 vcc, exec, s[38:39]
	v_min_f32_e32 v20, 0x437e0000, v20
	v_fmamk_f32 v20, v20, 0x3b808081, v245
	v_rcp_f32_e32 v20, v20
	s_nop 0
	v_cvt_pk_u8_f32 v18, v20, 2, v18
	v_fmamk_f32 v20, v90, 0xbb38aa3b, v8
	v_exp_f32_e32 v20, v20
	s_nop 0
	v_min_f32_e32 v20, 0x437e0000, v20
	v_fmamk_f32 v20, v20, 0x3b808081, v245
	v_rcp_f32_e32 v20, v20
	s_nop 0
	v_cvt_pk_u8_f32 v19, v20, 2, v19
	v_fmamk_f32 v20, v95, 0xbb38aa3b, v11
	v_exp_f32_e32 v20, v20
	s_nop 0
	v_min_f32_e32 v20, 0x437e0000, v20
	v_fmamk_f32 v20, v20, 0x3b808081, v245
	v_rcp_f32_e32 v20, v20
	s_nop 0
	v_cvt_pk_u8_f32 v18, v20, 3, v18
	v_fmamk_f32 v20, v91, 0xbb38aa3b, v9
	v_exp_f32_e32 v20, v20
	s_nop 0
	v_min_f32_e32 v20, 0x437e0000, v20
	v_fmamk_f32 v20, v20, 0x3b808081, v245
	v_rcp_f32_e32 v20, v20
	s_nop 0
	v_cvt_pk_u8_f32 v19, v20, 3, v19
	global_store_dwordx2 v[16:17], v[18:19], off
	v_fmamk_f32 v18, v84, 0xbb38aa3b, v6
	v_exp_f32_e32 v18, v18
	v_fmamk_f32 v20, v85, 0xbb38aa3b, v7
	v_exp_f32_e32 v20, v20
	v_fmamk_f32 v19, v80, 0xbb38aa3b, v4
	v_min_f32_e32 v18, 0x437e0000, v18
	v_fmamk_f32 v18, v18, 0x3b808081, v245
	v_min_f32_e32 v20, 0x437e0000, v20
	v_rcp_f32_e32 v18, v18
	v_fmamk_f32 v20, v20, 0x3b808081, v245
	v_rcp_f32_e32 v20, v20
	v_exp_f32_e32 v19, v19
	v_cvt_pk_u8_f32 v18, v18, 0, 0
	v_cvt_pk_u8_f32 v18, v20, 1, v18
	v_fmamk_f32 v20, v81, 0xbb38aa3b, v5
	v_exp_f32_e32 v20, v20
	v_min_f32_e32 v19, 0x437e0000, v19
	v_fmamk_f32 v19, v19, 0x3b808081, v245
	v_rcp_f32_e32 v19, v19
	v_min_f32_e32 v20, 0x437e0000, v20
	v_fmamk_f32 v20, v20, 0x3b808081, v245
	v_rcp_f32_e32 v20, v20
	v_cvt_pk_u8_f32 v19, v19, 0, 0
	v_cvt_pk_u8_f32 v19, v20, 1, v19
	v_fmamk_f32 v20, v86, 0xbb38aa3b, v2
	v_exp_f32_e32 v20, v20
	s_nop 0
	v_min_f32_e32 v20, 0x437e0000, v20
	v_fmamk_f32 v20, v20, 0x3b808081, v245
	v_rcp_f32_e32 v20, v20
	s_nop 0
	v_cvt_pk_u8_f32 v18, v20, 2, v18
	v_fmamk_f32 v20, v82, 0xbb38aa3b, v0
	v_exp_f32_e32 v20, v20
	s_nop 0
	v_min_f32_e32 v20, 0x437e0000, v20
	v_fmamk_f32 v20, v20, 0x3b808081, v245
	v_rcp_f32_e32 v20, v20
	s_nop 0
	v_cvt_pk_u8_f32 v19, v20, 2, v19
	v_fmamk_f32 v20, v87, 0xbb38aa3b, v3
	v_exp_f32_e32 v20, v20
	s_nop 0
	v_min_f32_e32 v20, 0x437e0000, v20
	v_fmamk_f32 v20, v20, 0x3b808081, v245
	v_rcp_f32_e32 v20, v20
	s_nop 0
	v_cvt_pk_u8_f32 v18, v20, 3, v18
	v_fmamk_f32 v20, v83, 0xbb38aa3b, v1
	v_exp_f32_e32 v20, v20
	s_nop 0
	v_min_f32_e32 v20, 0x437e0000, v20
	v_fmamk_f32 v20, v20, 0x3b808081, v245
	v_rcp_f32_e32 v20, v20
	s_nop 0
	v_cvt_pk_u8_f32 v19, v20, 3, v19
	global_store_dwordx2 v[16:17], v[18:19], off offset:512
	v_fmamk_f32 v18, v76, 0xbb38aa3b, v14
	v_exp_f32_e32 v18, v18
	v_fmamk_f32 v20, v77, 0xbb38aa3b, v15
	v_exp_f32_e32 v20, v20
	v_fmamk_f32 v19, v72, 0xbb38aa3b, v12
	v_min_f32_e32 v18, 0x437e0000, v18
	v_fmamk_f32 v18, v18, 0x3b808081, v245
	v_min_f32_e32 v20, 0x437e0000, v20
	v_rcp_f32_e32 v18, v18
	v_fmamk_f32 v20, v20, 0x3b808081, v245
	v_rcp_f32_e32 v20, v20
	v_exp_f32_e32 v19, v19
	v_cvt_pk_u8_f32 v18, v18, 0, 0
	v_cvt_pk_u8_f32 v18, v20, 1, v18
	v_fmamk_f32 v20, v73, 0xbb38aa3b, v13
	v_exp_f32_e32 v20, v20
	v_min_f32_e32 v19, 0x437e0000, v19
	v_fmamk_f32 v19, v19, 0x3b808081, v245
	v_rcp_f32_e32 v19, v19
	v_min_f32_e32 v20, 0x437e0000, v20
	v_fmamk_f32 v20, v20, 0x3b808081, v245
	v_rcp_f32_e32 v20, v20
	v_cvt_pk_u8_f32 v19, v19, 0, 0
	v_cvt_pk_u8_f32 v19, v20, 1, v19
	v_fmamk_f32 v20, v78, 0xbb38aa3b, v10
	v_exp_f32_e32 v20, v20
	s_nop 0
	v_min_f32_e32 v20, 0x437e0000, v20
	v_fmamk_f32 v20, v20, 0x3b808081, v245
	v_rcp_f32_e32 v20, v20
	s_nop 0
	v_cvt_pk_u8_f32 v18, v20, 2, v18
	v_fmamk_f32 v20, v74, 0xbb38aa3b, v8
	v_exp_f32_e32 v20, v20
	s_nop 0
	v_min_f32_e32 v20, 0x437e0000, v20
	v_fmamk_f32 v20, v20, 0x3b808081, v245
	v_rcp_f32_e32 v20, v20
	s_nop 0
	v_cvt_pk_u8_f32 v19, v20, 2, v19
	v_fmamk_f32 v20, v79, 0xbb38aa3b, v11
	v_exp_f32_e32 v20, v20
	s_nop 0
	v_min_f32_e32 v20, 0x437e0000, v20
	v_fmamk_f32 v20, v20, 0x3b808081, v245
	v_rcp_f32_e32 v20, v20
	s_nop 0
	v_cvt_pk_u8_f32 v18, v20, 3, v18
	v_fmamk_f32 v20, v75, 0xbb38aa3b, v9
	v_exp_f32_e32 v20, v20
	s_nop 0
	v_min_f32_e32 v20, 0x437e0000, v20
	v_fmamk_f32 v20, v20, 0x3b808081, v245
	v_rcp_f32_e32 v20, v20
	s_nop 0
	v_cvt_pk_u8_f32 v19, v20, 3, v19
	global_store_dwordx2 v[16:17], v[18:19], off offset:1024
	v_fmamk_f32 v18, v68, 0xbb38aa3b, v6
	v_exp_f32_e32 v18, v18
	v_fmamk_f32 v20, v69, 0xbb38aa3b, v7
	v_exp_f32_e32 v20, v20
	v_fmamk_f32 v19, v64, 0xbb38aa3b, v4
	v_min_f32_e32 v18, 0x437e0000, v18
	v_fmamk_f32 v18, v18, 0x3b808081, v245
	v_min_f32_e32 v20, 0x437e0000, v20
	v_rcp_f32_e32 v18, v18
	v_fmamk_f32 v20, v20, 0x3b808081, v245
	v_rcp_f32_e32 v20, v20
	v_exp_f32_e32 v19, v19
	v_cvt_pk_u8_f32 v18, v18, 0, 0
	v_cvt_pk_u8_f32 v18, v20, 1, v18
	v_fmamk_f32 v20, v65, 0xbb38aa3b, v5
	v_exp_f32_e32 v20, v20
	v_min_f32_e32 v19, 0x437e0000, v19
	v_fmamk_f32 v19, v19, 0x3b808081, v245
	v_rcp_f32_e32 v19, v19
	v_min_f32_e32 v20, 0x437e0000, v20
	v_fmamk_f32 v20, v20, 0x3b808081, v245
	v_rcp_f32_e32 v20, v20
	v_cvt_pk_u8_f32 v19, v19, 0, 0
	v_cvt_pk_u8_f32 v19, v20, 1, v19
	v_fmamk_f32 v20, v70, 0xbb38aa3b, v2
	v_exp_f32_e32 v20, v20
	s_nop 0
	v_min_f32_e32 v20, 0x437e0000, v20
	v_fmamk_f32 v20, v20, 0x3b808081, v245
	v_rcp_f32_e32 v20, v20
	s_nop 0
	v_cvt_pk_u8_f32 v18, v20, 2, v18
	v_fmamk_f32 v20, v66, 0xbb38aa3b, v0
	v_exp_f32_e32 v20, v20
	s_nop 0
	v_min_f32_e32 v20, 0x437e0000, v20
	v_fmamk_f32 v20, v20, 0x3b808081, v245
	v_rcp_f32_e32 v20, v20
	s_nop 0
	v_cvt_pk_u8_f32 v19, v20, 2, v19
	v_fmamk_f32 v20, v71, 0xbb38aa3b, v3
	v_exp_f32_e32 v20, v20
	s_nop 0
	v_min_f32_e32 v20, 0x437e0000, v20
	v_fmamk_f32 v20, v20, 0x3b808081, v245
	v_rcp_f32_e32 v20, v20
	s_nop 0
	v_cvt_pk_u8_f32 v18, v20, 3, v18
	v_fmamk_f32 v20, v67, 0xbb38aa3b, v1
	v_exp_f32_e32 v20, v20
	s_nop 0
	v_min_f32_e32 v20, 0x437e0000, v20
	v_fmamk_f32 v20, v20, 0x3b808081, v245
	v_rcp_f32_e32 v20, v20
	s_nop 0
	v_cvt_pk_u8_f32 v19, v20, 3, v19
	global_store_dwordx2 v[16:17], v[18:19], off offset:1536
	v_fmamk_f32 v18, v60, 0xbb38aa3b, v14
	v_exp_f32_e32 v18, v18
	v_fmamk_f32 v20, v61, 0xbb38aa3b, v15
	v_exp_f32_e32 v20, v20
	v_fmamk_f32 v19, v56, 0xbb38aa3b, v12
	v_min_f32_e32 v18, 0x437e0000, v18
	v_fmamk_f32 v18, v18, 0x3b808081, v245
	v_min_f32_e32 v20, 0x437e0000, v20
	v_rcp_f32_e32 v18, v18
	v_fmamk_f32 v20, v20, 0x3b808081, v245
	v_rcp_f32_e32 v20, v20
	v_exp_f32_e32 v19, v19
	v_cvt_pk_u8_f32 v18, v18, 0, 0
	v_fmamk_f32 v12, v40, 0xbb38aa3b, v12
	v_cvt_pk_u8_f32 v18, v20, 1, v18
	v_fmamk_f32 v20, v57, 0xbb38aa3b, v13
	v_exp_f32_e32 v20, v20
	v_min_f32_e32 v19, 0x437e0000, v19
	v_fmamk_f32 v19, v19, 0x3b808081, v245
	v_rcp_f32_e32 v19, v19
	v_min_f32_e32 v20, 0x437e0000, v20
	v_fmamk_f32 v20, v20, 0x3b808081, v245
	v_rcp_f32_e32 v20, v20
	v_cvt_pk_u8_f32 v19, v19, 0, 0
	v_exp_f32_e32 v12, v12
	v_fmac_f32_e32 v13, 0xbb38aa3b, v41
	v_cvt_pk_u8_f32 v19, v20, 1, v19
	v_fmamk_f32 v20, v62, 0xbb38aa3b, v10
	v_exp_f32_e32 v20, v20
	v_exp_f32_e32 v13, v13
	v_min_f32_e32 v12, 0x437e0000, v12
	v_fmamk_f32 v12, v12, 0x3b808081, v245
	v_min_f32_e32 v20, 0x437e0000, v20
	v_fmamk_f32 v20, v20, 0x3b808081, v245
	v_rcp_f32_e32 v20, v20
	v_min_f32_e32 v13, 0x437e0000, v13
	v_rcp_f32_e32 v12, v12
	v_fmamk_f32 v13, v13, 0x3b808081, v245
	v_cvt_pk_u8_f32 v18, v20, 2, v18
	v_fmamk_f32 v20, v58, 0xbb38aa3b, v8
	v_exp_f32_e32 v20, v20
	v_fmamk_f32 v8, v42, 0xbb38aa3b, v8
	v_exp_f32_e32 v8, v8
	v_rcp_f32_e32 v13, v13
	v_min_f32_e32 v20, 0x437e0000, v20
	v_fmamk_f32 v20, v20, 0x3b808081, v245
	v_rcp_f32_e32 v20, v20
	v_min_f32_e32 v8, 0x437e0000, v8
	v_fmamk_f32 v8, v8, 0x3b808081, v245
	v_fmamk_f32 v14, v44, 0xbb38aa3b, v14
	v_cvt_pk_u8_f32 v19, v20, 2, v19
	v_fmamk_f32 v20, v63, 0xbb38aa3b, v11
	v_exp_f32_e32 v20, v20
	v_rcp_f32_e32 v8, v8
	v_exp_f32_e32 v14, v14
	v_fmac_f32_e32 v15, 0xbb38aa3b, v45
	v_min_f32_e32 v20, 0x437e0000, v20
	v_fmamk_f32 v20, v20, 0x3b808081, v245
	v_rcp_f32_e32 v20, v20
	v_cvt_pk_u8_f32 v12, v12, 0, 0
	v_exp_f32_e32 v15, v15
	v_fmamk_f32 v10, v46, 0xbb38aa3b, v10
	v_cvt_pk_u8_f32 v18, v20, 3, v18
	v_fmamk_f32 v20, v59, 0xbb38aa3b, v9
	v_exp_f32_e32 v20, v20
	v_cvt_pk_u8_f32 v12, v13, 1, v12
	v_exp_f32_e32 v10, v10
	v_fmac_f32_e32 v11, 0xbb38aa3b, v47
	v_min_f32_e32 v20, 0x437e0000, v20
	v_fmamk_f32 v20, v20, 0x3b808081, v245
	v_rcp_f32_e32 v20, v20
	v_fmac_f32_e32 v9, 0xbb38aa3b, v43
	v_cvt_pk_u8_f32 v12, v8, 2, v12
	v_exp_f32_e32 v8, v11
	v_cvt_pk_u8_f32 v19, v20, 3, v19
	global_store_dwordx2 v[16:17], v[18:19], off offset:2048
	v_fmamk_f32 v18, v52, 0xbb38aa3b, v6
	v_exp_f32_e32 v18, v18
	v_fmamk_f32 v20, v53, 0xbb38aa3b, v7
	v_exp_f32_e32 v20, v20
	v_fmamk_f32 v19, v48, 0xbb38aa3b, v4
	v_min_f32_e32 v18, 0x437e0000, v18
	v_fmamk_f32 v18, v18, 0x3b808081, v245
	v_min_f32_e32 v20, 0x437e0000, v20
	v_rcp_f32_e32 v18, v18
	v_fmamk_f32 v20, v20, 0x3b808081, v245
	v_rcp_f32_e32 v20, v20
	v_exp_f32_e32 v19, v19
	v_cvt_pk_u8_f32 v18, v18, 0, 0
	v_fmamk_f32 v4, v32, 0xbb38aa3b, v4
	v_cvt_pk_u8_f32 v18, v20, 1, v18
	v_fmamk_f32 v20, v49, 0xbb38aa3b, v5
	v_exp_f32_e32 v20, v20
	v_min_f32_e32 v19, 0x437e0000, v19
	v_fmamk_f32 v19, v19, 0x3b808081, v245
	v_rcp_f32_e32 v19, v19
	v_min_f32_e32 v20, 0x437e0000, v20
	v_fmamk_f32 v20, v20, 0x3b808081, v245
	v_rcp_f32_e32 v20, v20
	v_cvt_pk_u8_f32 v19, v19, 0, 0
	v_exp_f32_e32 v4, v4
	v_fmac_f32_e32 v5, 0xbb38aa3b, v33
	v_cvt_pk_u8_f32 v19, v20, 1, v19
	v_fmamk_f32 v20, v54, 0xbb38aa3b, v2
	v_exp_f32_e32 v20, v20
	v_exp_f32_e32 v5, v5
	v_min_f32_e32 v4, 0x437e0000, v4
	v_fmamk_f32 v4, v4, 0x3b808081, v245
	v_min_f32_e32 v20, 0x437e0000, v20
	v_fmamk_f32 v20, v20, 0x3b808081, v245
	v_rcp_f32_e32 v20, v20
	v_min_f32_e32 v5, 0x437e0000, v5
	v_rcp_f32_e32 v4, v4
	v_fmamk_f32 v5, v5, 0x3b808081, v245
	v_cvt_pk_u8_f32 v18, v20, 2, v18
	v_fmamk_f32 v20, v50, 0xbb38aa3b, v0
	v_exp_f32_e32 v20, v20
	v_fmamk_f32 v0, v34, 0xbb38aa3b, v0
	v_exp_f32_e32 v0, v0
	v_rcp_f32_e32 v5, v5
	v_min_f32_e32 v20, 0x437e0000, v20
	v_fmamk_f32 v20, v20, 0x3b808081, v245
	v_rcp_f32_e32 v20, v20
	v_min_f32_e32 v0, 0x437e0000, v0
	v_fmamk_f32 v0, v0, 0x3b808081, v245
	v_fmamk_f32 v6, v36, 0xbb38aa3b, v6
	v_cvt_pk_u8_f32 v19, v20, 2, v19
	v_fmamk_f32 v20, v55, 0xbb38aa3b, v3
	v_exp_f32_e32 v20, v20
	v_rcp_f32_e32 v0, v0
	v_exp_f32_e32 v6, v6
	v_fmac_f32_e32 v7, 0xbb38aa3b, v37
	v_min_f32_e32 v20, 0x437e0000, v20
	v_fmamk_f32 v20, v20, 0x3b808081, v245
	v_rcp_f32_e32 v20, v20
	v_cvt_pk_u8_f32 v4, v4, 0, 0
	v_exp_f32_e32 v7, v7
	v_fmamk_f32 v2, v38, 0xbb38aa3b, v2
	v_cvt_pk_u8_f32 v18, v20, 3, v18
	v_fmamk_f32 v20, v51, 0xbb38aa3b, v1
	v_cvt_pk_u8_f32 v4, v5, 1, v4
	v_exp_f32_e32 v2, v2
	v_fmac_f32_e32 v3, 0xbb38aa3b, v39
	v_fmac_f32_e32 v1, 0xbb38aa3b, v35
	v_exp_f32_e32 v20, v20
	v_exp_f32_e32 v9, v9
	v_cvt_pk_u8_f32 v4, v0, 2, v4
	v_exp_f32_e32 v0, v3
	v_exp_f32_e32 v1, v1
	v_min_f32_e32 v14, 0x437e0000, v14
	v_min_f32_e32 v6, 0x437e0000, v6
	v_fmamk_f32 v14, v14, 0x3b808081, v245
	v_min_f32_e32 v15, 0x437e0000, v15
	v_fmamk_f32 v6, v6, 0x3b808081, v245
	v_min_f32_e32 v7, 0x437e0000, v7
	v_rcp_f32_e32 v14, v14
	v_fmamk_f32 v15, v15, 0x3b808081, v245
	v_min_f32_e32 v10, 0x437e0000, v10
	v_rcp_f32_e32 v6, v6
	v_fmamk_f32 v7, v7, 0x3b808081, v245
	v_min_f32_e32 v2, 0x437e0000, v2
	v_min_f32_e32 v20, 0x437e0000, v20
	v_rcp_f32_e32 v15, v15
	v_fmamk_f32 v10, v10, 0x3b808081, v245
	v_min_f32_e32 v8, 0x437e0000, v8
	v_min_f32_e32 v9, 0x437e0000, v9
	v_rcp_f32_e32 v7, v7
	v_fmamk_f32 v2, v2, 0x3b808081, v245
	v_min_f32_e32 v0, 0x437e0000, v0
	v_min_f32_e32 v1, 0x437e0000, v1
	v_fmamk_f32 v20, v20, 0x3b808081, v245
	v_rcp_f32_e32 v10, v10
	v_fmamk_f32 v8, v8, 0x3b808081, v245
	v_fmamk_f32 v9, v9, 0x3b808081, v245
	v_rcp_f32_e32 v2, v2
	v_fmamk_f32 v0, v0, 0x3b808081, v245
	v_fmamk_f32 v1, v1, 0x3b808081, v245
	v_rcp_f32_e32 v20, v20
	v_rcp_f32_e32 v8, v8
	v_rcp_f32_e32 v9, v9
	v_rcp_f32_e32 v0, v0
	v_rcp_f32_e32 v1, v1
	v_cvt_pk_u8_f32 v14, v14, 0, 0
	v_cvt_pk_u8_f32 v6, v6, 0, 0
	v_cvt_pk_u8_f32 v14, v15, 1, v14
	v_cvt_pk_u8_f32 v6, v7, 1, v6
	v_cvt_pk_u8_f32 v10, v10, 2, v14
	v_cvt_pk_u8_f32 v2, v2, 2, v6
	v_cvt_pk_u8_f32 v19, v20, 3, v19
	v_cvt_pk_u8_f32 v8, v8, 3, v10
	v_cvt_pk_u8_f32 v9, v9, 3, v12
	v_cvt_pk_u8_f32 v0, v0, 3, v2
	v_cvt_pk_u8_f32 v1, v1, 3, v4
	global_store_dwordx2 v[16:17], v[18:19], off offset:2560
	global_store_dwordx2 v[16:17], v[8:9], off offset:3072
	global_store_dwordx2 v[16:17], v[0:1], off offset:3584
	s_cbranch_vccnz .LBB0_769
	s_andn2_b64 vcc, exec, s[34:35]
	s_cbranch_vccnz .LBB0_768
	s_barrier
	s_branch .LBB0_768
